# v85 with packed f32 multiply (v_pk_mul_f32) for the x64 scaling in the in-loop converter
# baseline (speedup 1.0000x reference)
; #define LAS __attribute__((address_space(3)))
; __device__ __forceinline__ float clamp8(float x) { return __builtin_amdgcn_fmed3f(x, -448.f, 448.f); }
; __device__ __forceinline__ void cvt_finish(const CvtDesc& d, const float (&t)[64], LAS float* scr, int lane) {
;     ...
;     if (d.f8) {
; #pragma unroll
;         for (int j = 0; j < 8; ++j) { const int n = (lane >> 3) + 8 * j; const LAS float* s = scr + (8 * c) * 65 + n;
;             int a = __builtin_amdgcn_cvt_pk_fp8_f32(clamp8(s[0 * 65] * W8_SCALE), clamp8(s[1 * 65] * W8_SCALE), 0, false); a = __builtin_amdgcn_cvt_pk_fp8_f32(clamp8(s[2 * 65] * W8_SCALE), clamp8(s[3 * 65] * W8_SCALE), a, true);
;             int b = __builtin_amdgcn_cvt_pk_fp8_f32(clamp8(s[4 * 65] * W8_SCALE), clamp8(s[5 * 65] * W8_SCALE), 0, false); b = __builtin_amdgcn_cvt_pk_fp8_f32(clamp8(s[6 * 65] * W8_SCALE), clamp8(s[7 * 65] * W8_SCALE), b, true);
;             __builtin_nontemporal_store((u32x2){(unsigned)a, (unsigned)b}, (u32x2*)(d.dst + (size_t)n * d.dKB + 8 * c)); }
.Lilc_n_da:
	s_cmp_eq_u32 s42, 0
	s_cbranch_scc1 .Lilc_np_da
	s_mov_b32 s53, 4
	s_mov_b32 s46, 0x42800000
	v_pk_mul_f32 v[232:233], v[232:233], s[46:47] op_sel_hi:[1,0]
	v_pk_mul_f32 v[234:235], v[234:235], s[46:47] op_sel_hi:[1,0]
	v_pk_mul_f32 v[236:237], v[236:237], s[46:47] op_sel_hi:[1,0]
	v_pk_mul_f32 v[238:239], v[238:239], s[46:47] op_sel_hi:[1,0]
	v_pk_mul_f32 v[240:241], v[240:241], s[46:47] op_sel_hi:[1,0]
	v_pk_mul_f32 v[242:243], v[242:243], s[46:47] op_sel_hi:[1,0]
	v_pk_mul_f32 v[244:245], v[244:245], s[46:47] op_sel_hi:[1,0]
	v_pk_mul_f32 v[246:247], v[246:247], s[46:47] op_sel_hi:[1,0]
	v_pk_mul_f32 v[248:249], v[248:249], s[46:47] op_sel_hi:[1,0]
	v_pk_mul_f32 v[250:251], v[250:251], s[46:47] op_sel_hi:[1,0]
	v_pk_mul_f32 v[206:207], v[206:207], s[46:47] op_sel_hi:[1,0]
	v_pk_mul_f32 v[208:209], v[208:209], s[46:47] op_sel_hi:[1,0]
	v_pk_mul_f32 v[210:211], v[210:211], s[46:47] op_sel_hi:[1,0]
	v_pk_mul_f32 v[212:213], v[212:213], s[46:47] op_sel_hi:[1,0]
	v_pk_mul_f32 v[214:215], v[214:215], s[46:47] op_sel_hi:[1,0]
	v_pk_mul_f32 v[216:217], v[216:217], s[46:47] op_sel_hi:[1,0]
	v_med3_f32 v232, v232, s93, v224
	v_med3_f32 v233, v233, s93, v224
	v_med3_f32 v234, v234, s93, v224
	v_med3_f32 v235, v235, s93, v224
	v_med3_f32 v236, v236, s93, v224
	v_med3_f32 v237, v237, s93, v224
	v_med3_f32 v238, v238, s93, v224
	v_med3_f32 v239, v239, s93, v224
	v_med3_f32 v240, v240, s93, v224
	v_med3_f32 v241, v241, s93, v224
	v_med3_f32 v242, v242, s93, v224
	v_med3_f32 v243, v243, s93, v224
	v_med3_f32 v244, v244, s93, v224
	v_med3_f32 v245, v245, s93, v224
	v_med3_f32 v246, v246, s93, v224
	v_med3_f32 v247, v247, s93, v224
	v_med3_f32 v248, v248, s93, v224
	v_med3_f32 v249, v249, s93, v224
	v_med3_f32 v250, v250, s93, v224
	v_med3_f32 v251, v251, s93, v224
	v_med3_f32 v206, v206, s93, v224
	v_med3_f32 v207, v207, s93, v224
	v_med3_f32 v208, v208, s93, v224
	v_med3_f32 v209, v209, s93, v224
	v_med3_f32 v210, v210, s93, v224
	v_med3_f32 v211, v211, s93, v224
	v_med3_f32 v212, v212, s93, v224
	v_med3_f32 v213, v213, s93, v224
	v_med3_f32 v214, v214, s93, v224
	v_med3_f32 v215, v215, s93, v224
	v_med3_f32 v216, v216, s93, v224
	v_med3_f32 v217, v217, s93, v224
	v_lshlrev_b32_e32 v230, 3, v226
	v_lshl_add_u32 v225, v229, s42, v230
	v_cvt_pk_fp8_f32 v252, v232, v236
	v_cvt_pk_fp8_f32 v253, v248, v206
	v_cvt_pk_fp8_f32 v252, v240, v244 op_sel:[0,0,1]
	v_cvt_pk_fp8_f32 v253, v210, v214 op_sel:[0,0,1]
	s_nop 0
	global_store_dwordx2 v225, v[252:253], s[40:41] nt
	v_add_u32_e32 v225, s43, v225
	v_cvt_pk_fp8_f32 v252, v233, v237
	v_cvt_pk_fp8_f32 v253, v249, v207
	v_cvt_pk_fp8_f32 v252, v241, v245 op_sel:[0,0,1]
	v_cvt_pk_fp8_f32 v253, v211, v215 op_sel:[0,0,1]
	s_nop 0
	global_store_dwordx2 v225, v[252:253], s[40:41] nt
	v_add_u32_e32 v225, s43, v225
	v_cvt_pk_fp8_f32 v252, v234, v238
	v_cvt_pk_fp8_f32 v253, v250, v208
	v_cvt_pk_fp8_f32 v252, v242, v246 op_sel:[0,0,1]
	v_cvt_pk_fp8_f32 v253, v212, v216 op_sel:[0,0,1]
	s_nop 0
	global_store_dwordx2 v225, v[252:253], s[40:41] nt
	v_add_u32_e32 v225, s43, v225
	v_cvt_pk_fp8_f32 v252, v235, v239
	v_cvt_pk_fp8_f32 v253, v251, v209
	v_cvt_pk_fp8_f32 v252, v243, v247 op_sel:[0,0,1]
	v_cvt_pk_fp8_f32 v253, v213, v217 op_sel:[0,0,1]
	s_nop 0
	global_store_dwordx2 v225, v[252:253], s[40:41] nt
	s_mov_b32 s42, 0
	s_branch .Lilc_i_da

; #define LAS __attribute__((address_space(3)))
; __device__ __forceinline__ float clamp8(float x) { return __builtin_amdgcn_fmed3f(x, -448.f, 448.f); }
; __device__ __forceinline__ void cvt_finish(const CvtDesc& d, const float (&t)[64], LAS float* scr, int lane) {
;     ...
;     if (d.f8) {
; #pragma unroll
;         for (int j = 0; j < 8; ++j) { const int n = (lane >> 3) + 8 * j; const LAS float* s = scr + (8 * c) * 65 + n;
;             int a = __builtin_amdgcn_cvt_pk_fp8_f32(clamp8(s[0 * 65] * W8_SCALE), clamp8(s[1 * 65] * W8_SCALE), 0, false); a = __builtin_amdgcn_cvt_pk_fp8_f32(clamp8(s[2 * 65] * W8_SCALE), clamp8(s[3 * 65] * W8_SCALE), a, true);
;             int b = __builtin_amdgcn_cvt_pk_fp8_f32(clamp8(s[4 * 65] * W8_SCALE), clamp8(s[5 * 65] * W8_SCALE), 0, false); b = __builtin_amdgcn_cvt_pk_fp8_f32(clamp8(s[6 * 65] * W8_SCALE), clamp8(s[7 * 65] * W8_SCALE), b, true);
;             __builtin_nontemporal_store((u32x2){(unsigned)a, (unsigned)b}, (u32x2*)(d.dst + (size_t)n * d.dKB + 8 * c)); }
.LBB0_509:
	s_cmp_eq_u32 s42, 0
	s_cbranch_scc1 .Lilc_fd_da
	s_mov_b32 s46, 0x42800000
	v_pk_mul_f32 v[232:233], v[232:233], s[46:47] op_sel_hi:[1,0]
	v_pk_mul_f32 v[234:235], v[234:235], s[46:47] op_sel_hi:[1,0]
	v_pk_mul_f32 v[236:237], v[236:237], s[46:47] op_sel_hi:[1,0]
	v_pk_mul_f32 v[238:239], v[238:239], s[46:47] op_sel_hi:[1,0]
	v_pk_mul_f32 v[240:241], v[240:241], s[46:47] op_sel_hi:[1,0]
	v_pk_mul_f32 v[242:243], v[242:243], s[46:47] op_sel_hi:[1,0]
	v_pk_mul_f32 v[244:245], v[244:245], s[46:47] op_sel_hi:[1,0]
	v_pk_mul_f32 v[246:247], v[246:247], s[46:47] op_sel_hi:[1,0]
	v_pk_mul_f32 v[248:249], v[248:249], s[46:47] op_sel_hi:[1,0]
	v_pk_mul_f32 v[250:251], v[250:251], s[46:47] op_sel_hi:[1,0]
	v_pk_mul_f32 v[206:207], v[206:207], s[46:47] op_sel_hi:[1,0]
	v_pk_mul_f32 v[208:209], v[208:209], s[46:47] op_sel_hi:[1,0]
	v_pk_mul_f32 v[210:211], v[210:211], s[46:47] op_sel_hi:[1,0]
	v_pk_mul_f32 v[212:213], v[212:213], s[46:47] op_sel_hi:[1,0]
	v_pk_mul_f32 v[214:215], v[214:215], s[46:47] op_sel_hi:[1,0]
	v_pk_mul_f32 v[216:217], v[216:217], s[46:47] op_sel_hi:[1,0]
	v_med3_f32 v232, v232, s93, v224
	v_med3_f32 v233, v233, s93, v224
	v_med3_f32 v234, v234, s93, v224
	v_med3_f32 v235, v235, s93, v224
	v_med3_f32 v236, v236, s93, v224
	v_med3_f32 v237, v237, s93, v224
	v_med3_f32 v238, v238, s93, v224
	v_med3_f32 v239, v239, s93, v224
	v_med3_f32 v240, v240, s93, v224
	v_med3_f32 v241, v241, s93, v224
	v_med3_f32 v242, v242, s93, v224
	v_med3_f32 v243, v243, s93, v224
	v_med3_f32 v244, v244, s93, v224
	v_med3_f32 v245, v245, s93, v224
	v_med3_f32 v246, v246, s93, v224
	v_med3_f32 v247, v247, s93, v224
	v_med3_f32 v248, v248, s93, v224
	v_med3_f32 v249, v249, s93, v224
	v_med3_f32 v250, v250, s93, v224
	v_med3_f32 v251, v251, s93, v224
	v_med3_f32 v206, v206, s93, v224
	v_med3_f32 v207, v207, s93, v224
	v_med3_f32 v208, v208, s93, v224
	v_med3_f32 v209, v209, s93, v224
	v_med3_f32 v210, v210, s93, v224
	v_med3_f32 v211, v211, s93, v224
	v_med3_f32 v212, v212, s93, v224
	v_med3_f32 v213, v213, s93, v224
	v_med3_f32 v214, v214, s93, v224
	v_med3_f32 v215, v215, s93, v224
	v_med3_f32 v216, v216, s93, v224
	v_med3_f32 v217, v217, s93, v224
	v_lshlrev_b32_e32 v230, 3, v226
	v_lshl_add_u32 v225, v229, s42, v230
	v_cvt_pk_fp8_f32 v252, v232, v236
	v_cvt_pk_fp8_f32 v253, v248, v206
	v_cvt_pk_fp8_f32 v252, v240, v244 op_sel:[0,0,1]
	v_cvt_pk_fp8_f32 v253, v210, v214 op_sel:[0,0,1]
	s_nop 0
	global_store_dwordx2 v225, v[252:253], s[40:41] nt
	v_add_u32_e32 v225, s43, v225
	v_cvt_pk_fp8_f32 v252, v233, v237
	v_cvt_pk_fp8_f32 v253, v249, v207
	v_cvt_pk_fp8_f32 v252, v241, v245 op_sel:[0,0,1]
	v_cvt_pk_fp8_f32 v253, v211, v215 op_sel:[0,0,1]
	s_nop 0
	global_store_dwordx2 v225, v[252:253], s[40:41] nt
	v_add_u32_e32 v225, s43, v225
	v_cvt_pk_fp8_f32 v252, v234, v238
	v_cvt_pk_fp8_f32 v253, v250, v208
	v_cvt_pk_fp8_f32 v252, v242, v246 op_sel:[0,0,1]
	v_cvt_pk_fp8_f32 v253, v212, v216 op_sel:[0,0,1]
	s_nop 0
	global_store_dwordx2 v225, v[252:253], s[40:41] nt
	v_add_u32_e32 v225, s43, v225
	v_cvt_pk_fp8_f32 v252, v235, v239
	v_cvt_pk_fp8_f32 v253, v251, v209
	v_cvt_pk_fp8_f32 v252, v243, v247 op_sel:[0,0,1]
	v_cvt_pk_fp8_f32 v253, v213, v217 op_sel:[0,0,1]
	s_nop 0
	global_store_dwordx2 v225, v[252:253], s[40:41] nt
	s_mov_b32 s42, 0

; #define LAS __attribute__((address_space(3)))
; __device__ __forceinline__ float clamp8(float x) { return __builtin_amdgcn_fmed3f(x, -448.f, 448.f); }
; __device__ __forceinline__ void cvt_finish(const CvtDesc& d, const float (&t)[64], LAS float* scr, int lane) {
;     ...
;     if (d.f8) {
; #pragma unroll
;         for (int j = 0; j < 8; ++j) { const int n = (lane >> 3) + 8 * j; const LAS float* s = scr + (8 * c) * 65 + n;
;             int a = __builtin_amdgcn_cvt_pk_fp8_f32(clamp8(s[0 * 65] * W8_SCALE), clamp8(s[1 * 65] * W8_SCALE), 0, false); a = __builtin_amdgcn_cvt_pk_fp8_f32(clamp8(s[2 * 65] * W8_SCALE), clamp8(s[3 * 65] * W8_SCALE), a, true);
;             int b = __builtin_amdgcn_cvt_pk_fp8_f32(clamp8(s[4 * 65] * W8_SCALE), clamp8(s[5 * 65] * W8_SCALE), 0, false); b = __builtin_amdgcn_cvt_pk_fp8_f32(clamp8(s[6 * 65] * W8_SCALE), clamp8(s[7 * 65] * W8_SCALE), b, true);
;             __builtin_nontemporal_store((u32x2){(unsigned)a, (unsigned)b}, (u32x2*)(d.dst + (size_t)n * d.dKB + 8 * c)); }
.Lilc_p_m:
	s_mov_b32 s53, 4
	s_mov_b32 s46, 0x42800000
	v_pk_mul_f32 v[232:233], v[232:233], s[46:47] op_sel_hi:[1,0]
	v_pk_mul_f32 v[234:235], v[234:235], s[46:47] op_sel_hi:[1,0]
	v_pk_mul_f32 v[236:237], v[236:237], s[46:47] op_sel_hi:[1,0]
	v_pk_mul_f32 v[238:239], v[238:239], s[46:47] op_sel_hi:[1,0]
	v_pk_mul_f32 v[240:241], v[240:241], s[46:47] op_sel_hi:[1,0]
	v_pk_mul_f32 v[242:243], v[242:243], s[46:47] op_sel_hi:[1,0]
	v_pk_mul_f32 v[244:245], v[244:245], s[46:47] op_sel_hi:[1,0]
	v_pk_mul_f32 v[246:247], v[246:247], s[46:47] op_sel_hi:[1,0]
	v_pk_mul_f32 v[248:249], v[248:249], s[46:47] op_sel_hi:[1,0]
	v_pk_mul_f32 v[250:251], v[250:251], s[46:47] op_sel_hi:[1,0]
	v_pk_mul_f32 v[206:207], v[206:207], s[46:47] op_sel_hi:[1,0]
	v_pk_mul_f32 v[208:209], v[208:209], s[46:47] op_sel_hi:[1,0]
	v_pk_mul_f32 v[210:211], v[210:211], s[46:47] op_sel_hi:[1,0]
	v_pk_mul_f32 v[212:213], v[212:213], s[46:47] op_sel_hi:[1,0]
	v_pk_mul_f32 v[214:215], v[214:215], s[46:47] op_sel_hi:[1,0]
	v_pk_mul_f32 v[216:217], v[216:217], s[46:47] op_sel_hi:[1,0]
	v_med3_f32 v232, v232, s93, v224
	v_med3_f32 v233, v233, s93, v224
	v_med3_f32 v234, v234, s93, v224
	v_med3_f32 v235, v235, s93, v224
	v_med3_f32 v236, v236, s93, v224
	v_med3_f32 v237, v237, s93, v224
	v_med3_f32 v238, v238, s93, v224
	v_med3_f32 v239, v239, s93, v224
	v_med3_f32 v240, v240, s93, v224
	v_med3_f32 v241, v241, s93, v224
	v_med3_f32 v242, v242, s93, v224
	v_med3_f32 v243, v243, s93, v224
	v_med3_f32 v244, v244, s93, v224
	v_med3_f32 v245, v245, s93, v224
	v_med3_f32 v246, v246, s93, v224
	v_med3_f32 v247, v247, s93, v224
	v_med3_f32 v248, v248, s93, v224
	v_med3_f32 v249, v249, s93, v224
	v_med3_f32 v250, v250, s93, v224
	v_med3_f32 v251, v251, s93, v224
	v_med3_f32 v206, v206, s93, v224
	v_med3_f32 v207, v207, s93, v224
	v_med3_f32 v208, v208, s93, v224
	v_med3_f32 v209, v209, s93, v224
	v_med3_f32 v210, v210, s93, v224
	v_med3_f32 v211, v211, s93, v224
	v_med3_f32 v212, v212, s93, v224
	v_med3_f32 v213, v213, s93, v224
	v_med3_f32 v214, v214, s93, v224
	v_med3_f32 v215, v215, s93, v224
	v_med3_f32 v216, v216, s93, v224
	v_med3_f32 v217, v217, s93, v224
	v_lshlrev_b32_e32 v230, 3, v226
	v_lshl_add_u32 v225, v229, s42, v230
	v_cvt_pk_fp8_f32 v252, v232, v236
	v_cvt_pk_fp8_f32 v253, v248, v206
	v_cvt_pk_fp8_f32 v252, v240, v244 op_sel:[0,0,1]
	v_cvt_pk_fp8_f32 v253, v210, v214 op_sel:[0,0,1]
	s_nop 0
	global_store_dwordx2 v225, v[252:253], s[40:41] nt
	v_add_u32_e32 v225, s43, v225
	v_cvt_pk_fp8_f32 v252, v233, v237
	v_cvt_pk_fp8_f32 v253, v249, v207
	v_cvt_pk_fp8_f32 v252, v241, v245 op_sel:[0,0,1]
	v_cvt_pk_fp8_f32 v253, v211, v215 op_sel:[0,0,1]
	s_nop 0
	global_store_dwordx2 v225, v[252:253], s[40:41] nt
	v_add_u32_e32 v225, s43, v225
	v_cvt_pk_fp8_f32 v252, v234, v238
	v_cvt_pk_fp8_f32 v253, v250, v208
	v_cvt_pk_fp8_f32 v252, v242, v246 op_sel:[0,0,1]
	v_cvt_pk_fp8_f32 v253, v212, v216 op_sel:[0,0,1]
	s_nop 0
	global_store_dwordx2 v225, v[252:253], s[40:41] nt
	v_add_u32_e32 v225, s43, v225
	v_cvt_pk_fp8_f32 v252, v235, v239
	v_cvt_pk_fp8_f32 v253, v251, v209
	v_cvt_pk_fp8_f32 v252, v243, v247 op_sel:[0,0,1]
	v_cvt_pk_fp8_f32 v253, v213, v217 op_sel:[0,0,1]
	s_nop 0
	global_store_dwordx2 v225, v[252:253], s[40:41] nt
	s_mov_b32 s42, 0
	s_branch .Lilc_i_m

; #define LAS __attribute__((address_space(3)))
; __device__ __forceinline__ float clamp8(float x) { return __builtin_amdgcn_fmed3f(x, -448.f, 448.f); }
; #define VM_WAIT() asm volatile("s_waitcnt vmcnt(0)" ::: "memory")
;     ...
;             VM_WAIT();
;             __syncthreads();
;         }
; __device__ __forceinline__ void cvt_finish(const CvtDesc& d, const float (&t)[64], LAS float* scr, int lane) {
;     ...
;     if (d.f8) {
; #pragma unroll
;         for (int j = 0; j < 8; ++j) { const int n = (lane >> 3) + 8 * j; const LAS float* s = scr + (8 * c) * 65 + n;
;             int a = __builtin_amdgcn_cvt_pk_fp8_f32(clamp8(s[0 * 65] * W8_SCALE), clamp8(s[1 * 65] * W8_SCALE), 0, false); a = __builtin_amdgcn_cvt_pk_fp8_f32(clamp8(s[2 * 65] * W8_SCALE), clamp8(s[3 * 65] * W8_SCALE), a, true);
;             int b = __builtin_amdgcn_cvt_pk_fp8_f32(clamp8(s[4 * 65] * W8_SCALE), clamp8(s[5 * 65] * W8_SCALE), 0, false); b = __builtin_amdgcn_cvt_pk_fp8_f32(clamp8(s[6 * 65] * W8_SCALE), clamp8(s[7 * 65] * W8_SCALE), b, true);
;             __builtin_nontemporal_store((u32x2){(unsigned)a, (unsigned)b}, (u32x2*)(d.dst + (size_t)n * d.dKB + 8 * c)); }
.Lilc_wd_m:
	s_cmp_eq_u32 s28, 64
	s_barrier
	v_mfma_f32_32x32x16_bf16 v[48:63], v[70:73], v[86:89], v[48:63]
	v_mfma_f32_32x32x16_bf16 v[48:63], v[74:77], v[90:93], v[48:63]
	v_mfma_f32_32x32x16_bf16 v[48:63], v[78:81], v[174:177], v[48:63]
	s_cbranch_scc0 .LBB0_786
	s_cmp_eq_u32 s42, 0
	s_cbranch_scc1 .Lilc_fd_m
	s_waitcnt vmcnt(0)
	s_mov_b32 s46, 0x42800000
	v_pk_mul_f32 v[232:233], v[232:233], s[46:47] op_sel_hi:[1,0]
	v_pk_mul_f32 v[234:235], v[234:235], s[46:47] op_sel_hi:[1,0]
	v_pk_mul_f32 v[236:237], v[236:237], s[46:47] op_sel_hi:[1,0]
	v_pk_mul_f32 v[238:239], v[238:239], s[46:47] op_sel_hi:[1,0]
	v_pk_mul_f32 v[240:241], v[240:241], s[46:47] op_sel_hi:[1,0]
	v_pk_mul_f32 v[242:243], v[242:243], s[46:47] op_sel_hi:[1,0]
	v_pk_mul_f32 v[244:245], v[244:245], s[46:47] op_sel_hi:[1,0]
	v_pk_mul_f32 v[246:247], v[246:247], s[46:47] op_sel_hi:[1,0]
	v_pk_mul_f32 v[248:249], v[248:249], s[46:47] op_sel_hi:[1,0]
	v_pk_mul_f32 v[250:251], v[250:251], s[46:47] op_sel_hi:[1,0]
	v_pk_mul_f32 v[206:207], v[206:207], s[46:47] op_sel_hi:[1,0]
	v_pk_mul_f32 v[208:209], v[208:209], s[46:47] op_sel_hi:[1,0]
	v_pk_mul_f32 v[210:211], v[210:211], s[46:47] op_sel_hi:[1,0]
	v_pk_mul_f32 v[212:213], v[212:213], s[46:47] op_sel_hi:[1,0]
	v_pk_mul_f32 v[214:215], v[214:215], s[46:47] op_sel_hi:[1,0]
	v_pk_mul_f32 v[216:217], v[216:217], s[46:47] op_sel_hi:[1,0]
	v_med3_f32 v232, v232, s93, v224
	v_med3_f32 v233, v233, s93, v224
	v_med3_f32 v234, v234, s93, v224
	v_med3_f32 v235, v235, s93, v224
	v_med3_f32 v236, v236, s93, v224
	v_med3_f32 v237, v237, s93, v224
	v_med3_f32 v238, v238, s93, v224
	v_med3_f32 v239, v239, s93, v224
	v_med3_f32 v240, v240, s93, v224
	v_med3_f32 v241, v241, s93, v224
	v_med3_f32 v242, v242, s93, v224
	v_med3_f32 v243, v243, s93, v224
	v_med3_f32 v244, v244, s93, v224
	v_med3_f32 v245, v245, s93, v224
	v_med3_f32 v246, v246, s93, v224
	v_med3_f32 v247, v247, s93, v224
	v_med3_f32 v248, v248, s93, v224
	v_med3_f32 v249, v249, s93, v224
	v_med3_f32 v250, v250, s93, v224
	v_med3_f32 v251, v251, s93, v224
	v_med3_f32 v206, v206, s93, v224
	v_med3_f32 v207, v207, s93, v224
	v_med3_f32 v208, v208, s93, v224
	v_med3_f32 v209, v209, s93, v224
	v_med3_f32 v210, v210, s93, v224
	v_med3_f32 v211, v211, s93, v224
	v_med3_f32 v212, v212, s93, v224
	v_med3_f32 v213, v213, s93, v224
	v_med3_f32 v214, v214, s93, v224
	v_med3_f32 v215, v215, s93, v224
	v_med3_f32 v216, v216, s93, v224
	v_med3_f32 v217, v217, s93, v224
	v_lshlrev_b32_e32 v230, 3, v226
	v_lshl_add_u32 v225, v229, s42, v230
	v_cvt_pk_fp8_f32 v252, v232, v236
	v_cvt_pk_fp8_f32 v253, v248, v206
	v_cvt_pk_fp8_f32 v252, v240, v244 op_sel:[0,0,1]
	v_cvt_pk_fp8_f32 v253, v210, v214 op_sel:[0,0,1]
	s_nop 0
	global_store_dwordx2 v225, v[252:253], s[40:41] nt
	v_add_u32_e32 v225, s43, v225
	v_cvt_pk_fp8_f32 v252, v233, v237
	v_cvt_pk_fp8_f32 v253, v249, v207
	v_cvt_pk_fp8_f32 v252, v241, v245 op_sel:[0,0,1]
	v_cvt_pk_fp8_f32 v253, v211, v215 op_sel:[0,0,1]
	s_nop 0
	global_store_dwordx2 v225, v[252:253], s[40:41] nt
	v_add_u32_e32 v225, s43, v225
	v_cvt_pk_fp8_f32 v252, v234, v238
	v_cvt_pk_fp8_f32 v253, v250, v208
	v_cvt_pk_fp8_f32 v252, v242, v246 op_sel:[0,0,1]
	v_cvt_pk_fp8_f32 v253, v212, v216 op_sel:[0,0,1]
	s_nop 0
	global_store_dwordx2 v225, v[252:253], s[40:41] nt
	v_add_u32_e32 v225, s43, v225
	v_cvt_pk_fp8_f32 v252, v235, v239
	v_cvt_pk_fp8_f32 v253, v251, v209
	v_cvt_pk_fp8_f32 v252, v243, v247 op_sel:[0,0,1]
	v_cvt_pk_fp8_f32 v253, v213, v217 op_sel:[0,0,1]
	s_nop 0
	global_store_dwordx2 v225, v[252:253], s[40:41] nt
	s_mov_b32 s42, 0
